# 32 conversion sub-queues instead of 16
# speedup vs baseline: 1.0115x; 1.0115x over previous
; #define LAS __attribute__((address_space(3)))
; DI kptr_t kargs_now() { kptr_t p = (kptr_t)__builtin_amdgcn_kernarg_segment_ptr(); asm volatile("" : "+s"(p)); return p; }
; #define RI_NEXT(D_) do { if (q.cnt == 8) { int b_ = 0; if (F.lane == 0) b_ = (int)__hip_atomic_fetch_add(qctr, 8u, __ATOMIC_RELAXED, __HIP_MEMORY_SCOPE_AGENT); q.base = __builtin_amdgcn_readfirstlane(b_); q.cnt = 0; } \
;         D_ = decode_item(KA, F.ws, kind, q.base + q.cnt); ++q.cnt; } while (0)
; DI void run_items1(Frame& F, int kind, int quota, QState& q) {
;     const kptr_t KA = kargs_now();
;     LAS float* scr = (LAS float*)(F.lds + F.wave * 16384);
;     unsigned* qctr = F.ctl + CW_QUEUE + 64 * kind;
;     ...
;     if (quota == 0) return;
;     TItem d; RI_NEXT(d); if (!d.valid) return;
; DI void phase_attn(Frame& F, int l) {
;     ...
;     QState cq; cq.base = 0; cq.cnt = 8;
;     constexpr int SLOT_ITEMS = 3;
;     if (F.bid & 1) { __syncthreads(); run_items1(F, 1 + l, SLOT_ITEMS, cq); }
.LBB0_398:
	v_readlane_b32 s8, v255, 14
	v_readlane_b32 s4, v253, 8
	s_lshl_b32 s58, s8, 6
	v_readlane_b32 s6, v253, 10
	v_readlane_b32 s7, v253, 11
	s_lshl_b64 s[0:1], s[58:59], 2
	s_mov_b64 s[2:3], s[6:7]
	s_add_u32 s0, s2, s0
	s_addc_u32 s1, s3, s1
	v_readlane_b32 s9, v255, 15
	s_add_u32 s12, s0, 0x8100
	s_addc_u32 s13, s1, 0
	v_readlane_b32 s100, v253, 29
	s_lshr_b32 s100, s100, 1
	s_and_b32 s100, s100, 31
	s_lshl_b32 s0, s100, 8
	s_mul_i32 s1, s8, 0x1f00
	s_add_i32 s0, s0, s1
	s_add_i32 s0, s0, 0x2300
	s_add_u32 s12, s12, s0
	s_addc_u32 s13, s13, 0
	s_lshl_b64 s[0:1], s[8:9], 25
	v_writelane_b32 v255, s0, 16
	s_lshl_b64 s[62:63], s[8:9], 5
	s_lshl_b32 s2, s8, 20
	v_writelane_b32 v255, s1, 17
	s_mov_b32 s3, s59
	v_readlane_b32 s0, v253, 33
	v_writelane_b32 v255, s2, 18
	s_add_u32 s76, s0, s2
	v_readlane_b32 s0, v253, 34
	v_writelane_b32 v255, s3, 19
	s_addc_u32 s77, s0, 0
	s_lshl_b64 s[20:21], s[8:9], 21
	s_lshl_b64 s[0:1], s[8:9], 20
	v_readlane_b32 s2, v253, 35
	s_add_u32 s22, s2, s0
	v_readlane_b32 s2, v253, 36
	s_addc_u32 s23, s2, s1
	v_readlane_b32 s2, v253, 37
	s_add_u32 s24, s2, s0
	v_readlane_b32 s0, v253, 38
	s_addc_u32 s25, s0, s1
	s_lshl_b64 s[26:27], s[8:9], 24
	v_readlane_b32 s0, v253, 39
	s_add_u32 s14, s0, s44
	v_readlane_b32 s0, v253, 40
	s_addc_u32 s15, s0, s45
	s_mov_b32 s0, -1
	s_mov_b32 s95, 0
	v_mbcnt_lo_u32_b32 v0, s0, 0
	v_mbcnt_hi_u32_b32 v186, s0, v0
	v_readlane_b32 s0, v253, 29
	s_mov_b32 s51, s0
	s_mov_b64 s[30:31], s[70:71]
	s_bitcmp0_b32 s51, 0
	s_mov_b32 s63, 4
	v_readlane_b32 s5, v253, 9
	v_readlane_b32 s1, v253, 30
	s_cbranch_scc1 .LBB0_472
	s_mov_b64 s[6:7], s[70:71]
	v_mov_b32_e32 v0, 0
	v_cmp_eq_u32_e64 s[4:5], 0, v186
	s_waitcnt vmcnt(63) expcnt(7) lgkmcnt(15)
	s_barrier
	s_and_saveexec_b64 s[2:3], s[4:5]
	s_cbranch_execz .LBB0_403
	s_mov_b64 s[10:11], exec
	v_mbcnt_lo_u32_b32 v0, s10, 0
	v_mbcnt_hi_u32_b32 v0, s11, v0
	v_cmp_eq_u32_e32 vcc, 0, v0
	s_and_saveexec_b64 s[8:9], vcc
	s_cbranch_execz .LBB0_402
	s_bcnt1_i32_b64 s0, s[10:11]
	s_lshl_b32 s0, s0, 2
	v_mov_b32_e32 v2, s0
	global_atomic_add v2, v1, v2, s[12:13] sc0

; DI const float* inp(kptr_t k, int i) { return (const float*)k[i]; }
; DI int imap(int n, int H) { return ((n % H) / 128) * 256 + (n / H) * 128 + (n % 128); }
; DI TItem decode_item(kptr_t KA, unsigned char* ws, int kind, int it) {
;     TItem d; d.valid = it < (kind == 0 ? DEPTH * IT_SMALL : IT_EXP); if (!d.valid) it = 0;
;     const int l = kind == 0 ? it / IT_SMALL : kind - 1; int r = kind == 0 ? it % IT_SMALL : IT_SMALL + it;
;     const float* W; unsigned char* WT; int K, N, H = 0; bool f8 = false;
;     int nsub = 0, Kd = 0, kofs = 0;
;     if (r < IT_IN) { W = inp(KA, I_WIN) + (size_t)l * D * INW; K = D; N = INW;
;         WT = ws + WS_WIN + (size_t)l * INW * D; f8 = true; }
;     else if ((r -= IT_IN) < IT_GLU) { W = inp(KA, I_WGLU) + (size_t)l * SW * 1024; WT = ws + WS_WGLU + (size_t)l * 1024 * SW * 2; K = SW; N = 1024; H = 512; }
;     else if ((r -= IT_GLU) < IT_ATT) { W = inp(KA, I_WATTO) + (size_t)l * AW * D; WT = ws + WS_WCAT + (size_t)l * D * D; K = AW; N = D; Kd = D; f8 = true; }
;     else if ((r -= IT_ATT) < IT_SSMO) { W = inp(KA, I_WSSMO) + (size_t)l * SW * D; WT = ws + WS_WCAT + (size_t)l * D * D; K = SW; N = D; Kd = D; kofs = AW; f8 = true; }
;     else if ((r -= IT_SSMO) < IT_OUT) { W = inp(KA, I_WOUT) + (size_t)l * D * D; WT = ws + WS_WOUT + (size_t)l * D * D; K = D; N = D; f8 = true; }
;     else if ((r -= IT_OUT) < NE * IT_W1) { const int e = r / IT_W1; r %= IT_W1; W = inp(KA, I_WEXPIN) + ((size_t)l * NE + e) * D * 2048; WT = ws + WS_W1 + ((size_t)l * NE + e) * 2048 * D; K = D; N = 2048; H = 1024; f8 = true; }
;     else { r -= NE * IT_W1; const int e = r / IT_W2; r %= IT_W2; W = inp(KA, I_WEXPOUT) + ((size_t)l * NE + e) * DFF * D; WT = ws + WS_W2 + ((size_t)l * NE + e) * D * DFF; K = DFF; N = D; f8 = true; }
;     const int nblk = N / 64, kb = r / nblk, nb = r % nblk, n0 = nb * 64;
;     d.W = W; d.WT = WT; d.N = N; d.Kd = Kd ? Kd : K; d.kofs = kofs; d.drow0 = (H ? imap(n0, H) : n0) - nsub; d.k0 = kb * 64; d.n0 = n0; d.f8 = f8;
.LBB0_403:
	s_or_b64 exec, exec, s[2:3]
	v_readfirstlane_b32 s95, v0
	s_lshl_b32 s101, s95, 5
	s_or_b32 s101, s101, s100
	s_cmpk_lt_i32 s101, 0x6000
	s_cselect_b64 s[2:3], -1, 0
	s_and_b64 s[0:1], s[2:3], exec
	s_cselect_b32 s36, s101, 0
	s_add_i32 s0, s36, 0x680
	s_cmpk_gt_i32 s36, 0xfd7f
	s_mov_b64 s[18:19], -1
	s_cbranch_scc0 .LBB0_424
	s_mov_b64 s[34:35], -1
	s_cmpk_gt_u32 s0, 0x47f
	s_mov_b64 s[8:9], -1
	s_cbranch_scc0 .LBB0_421
	s_cmpk_gt_u32 s0, 0x4ff
	s_cbranch_scc0 .LBB0_418
	s_cmpk_gt_u32 s0, 0x57f
	s_cbranch_scc0 .LBB0_415
	s_cmp_lt_u32 s36, 0xfffff980
	s_cbranch_scc0 .LBB0_412
	s_mov_b64 s[28:29], -1
	s_cmpk_gt_u32 s0, 0x467f
	s_cbranch_scc0 .LBB0_410
	s_add_i32 s1, s36, 0xffffc000
	s_lshr_b32 s58, s1, 8
	s_load_dwordx2 s[8:9], s[6:7], 0xd0
	s_and_b32 s1, s36, 0xff
	s_lshl_b64 s[10:11], s[58:59], 20
	v_readlane_b32 s16, v255, 16
	v_readlane_b32 s17, v255, 17
	s_add_u32 s10, s10, s16
	s_addc_u32 s11, s11, s17
	s_lshl_b64 s[16:17], s[10:11], 2
	s_waitcnt lgkmcnt(0)
	s_add_u32 s16, s8, s16
	s_addc_u32 s17, s9, s17
	v_readlane_b32 s8, v253, 45
	s_add_u32 s10, s8, s10
	v_readlane_b32 s8, v253, 46
	s_addc_u32 s11, s8, s11
	s_mov_b64 s[8:9], 0

; DI const float* inp(kptr_t k, int i) { return (const float*)k[i]; }
; DI int imap(int n, int H) { return ((n % H) / 128) * 256 + (n / H) * 128 + (n % 128); }
; DI TItem decode_item(kptr_t KA, unsigned char* ws, int kind, int it) {
;     TItem d; d.valid = it < (kind == 0 ? DEPTH * IT_SMALL : IT_EXP); if (!d.valid) it = 0;
;     const int l = kind == 0 ? it / IT_SMALL : kind - 1; int r = kind == 0 ? it % IT_SMALL : IT_SMALL + it;
;     const float* W; unsigned char* WT; int K, N, H = 0; bool f8 = false;
;     int nsub = 0, Kd = 0, kofs = 0;
;     if (r < IT_IN) { W = inp(KA, I_WIN) + (size_t)l * D * INW; K = D; N = INW;
;         WT = ws + WS_WIN + (size_t)l * INW * D; f8 = true; }
;     else if ((r -= IT_IN) < IT_GLU) { W = inp(KA, I_WGLU) + (size_t)l * SW * 1024; WT = ws + WS_WGLU + (size_t)l * 1024 * SW * 2; K = SW; N = 1024; H = 512; }
;     else if ((r -= IT_GLU) < IT_ATT) { W = inp(KA, I_WATTO) + (size_t)l * AW * D; WT = ws + WS_WCAT + (size_t)l * D * D; K = AW; N = D; Kd = D; f8 = true; }
;     else if ((r -= IT_ATT) < IT_SSMO) { W = inp(KA, I_WSSMO) + (size_t)l * SW * D; WT = ws + WS_WCAT + (size_t)l * D * D; K = SW; N = D; Kd = D; kofs = AW; f8 = true; }
;     else if ((r -= IT_SSMO) < IT_OUT) { W = inp(KA, I_WOUT) + (size_t)l * D * D; WT = ws + WS_WOUT + (size_t)l * D * D; K = D; N = D; f8 = true; }
;     else if ((r -= IT_OUT) < NE * IT_W1) { const int e = r / IT_W1; r %= IT_W1; W = inp(KA, I_WEXPIN) + ((size_t)l * NE + e) * D * 2048; WT = ws + WS_W1 + ((size_t)l * NE + e) * 2048 * D; K = D; N = 2048; H = 1024; f8 = true; }
;     else { r -= NE * IT_W1; const int e = r / IT_W2; r %= IT_W2; W = inp(KA, I_WEXPOUT) + ((size_t)l * NE + e) * DFF * D; WT = ws + WS_W2 + ((size_t)l * NE + e) * D * DFF; K = DFF; N = D; f8 = true; }
;     const int nblk = N / 64, kb = r / nblk, nb = r % nblk, n0 = nb * 64;
;     d.W = W; d.WT = WT; d.N = N; d.Kd = Kd ? Kd : K; d.kofs = kofs; d.drow0 = (H ? imap(n0, H) : n0) - nsub; d.k0 = kb * 64; d.n0 = n0; d.f8 = f8;
.LBB0_437:
	s_add_i32 s9, s63, s95
	s_lshl_b32 s9, s9, 5
	s_or_b32 s9, s9, s100
	s_cmpk_lt_i32 s9, 0x6000
	s_cselect_b64 s[2:3], -1, 0
	s_and_b64 s[0:1], s[2:3], exec
	s_cselect_b32 s9, s9, 0
	s_add_i32 s0, s9, 0x680
	s_cmpk_gt_i32 s9, 0xfd7f
	s_mov_b64 s[18:19], -1
	s_cbranch_scc0 .LBB0_458
	s_mov_b64 s[16:17], -1
	s_cmpk_gt_u32 s0, 0x47f
	s_cbranch_scc0 .LBB0_455
	s_cmpk_gt_u32 s0, 0x4ff
	s_cbranch_scc0 .LBB0_452
	s_cmpk_gt_u32 s0, 0x57f
	s_cbranch_scc0 .LBB0_449
	s_cmp_lt_u32 s9, 0xfffff980
	s_cbranch_scc0 .LBB0_446
	s_mov_b64 s[56:57], -1
	s_cmpk_gt_u32 s0, 0x467f
	s_cbranch_scc0 .LBB0_444
	s_add_i32 s1, s9, 0xffffc000
	s_lshr_b32 s58, s1, 8
	s_load_dwordx2 s[18:19], s[6:7], 0xd0
	s_and_b32 s1, s9, 0xff
	s_lshl_b64 s[28:29], s[58:59], 20
	v_readlane_b32 s36, v255, 16
	v_readlane_b32 s37, v255, 17
	s_add_u32 s28, s28, s36
	s_addc_u32 s29, s29, s37
	s_lshl_b64 s[36:37], s[28:29], 2
	s_waitcnt lgkmcnt(0)
	s_add_u32 s42, s18, s36
	s_addc_u32 s43, s19, s37
	v_readlane_b32 s18, v253, 45
	s_add_u32 s28, s18, s28
	v_readlane_b32 s18, v253, 46
	s_addc_u32 s29, s18, s29
	s_mov_b64 s[18:19], 0

; DI const float* inp(kptr_t k, int i) { return (const float*)k[i]; }
; DI int imap(int n, int H) { return ((n % H) / 128) * 256 + (n / H) * 128 + (n % 128); }
; DI TItem decode_item(kptr_t KA, unsigned char* ws, int kind, int it) {
;     TItem d; d.valid = it < (kind == 0 ? DEPTH * IT_SMALL : IT_EXP); if (!d.valid) it = 0;
;     const int l = kind == 0 ? it / IT_SMALL : kind - 1; int r = kind == 0 ? it % IT_SMALL : IT_SMALL + it;
;     const float* W; unsigned char* WT; int K, N, H = 0; bool f8 = false;
;     int nsub = 0, Kd = 0, kofs = 0;
;     if (r < IT_IN) { W = inp(KA, I_WIN) + (size_t)l * D * INW; K = D; N = INW;
;         WT = ws + WS_WIN + (size_t)l * INW * D; f8 = true; }
;     else if ((r -= IT_IN) < IT_GLU) { W = inp(KA, I_WGLU) + (size_t)l * SW * 1024; WT = ws + WS_WGLU + (size_t)l * 1024 * SW * 2; K = SW; N = 1024; H = 512; }
;     else if ((r -= IT_GLU) < IT_ATT) { W = inp(KA, I_WATTO) + (size_t)l * AW * D; WT = ws + WS_WCAT + (size_t)l * D * D; K = AW; N = D; Kd = D; f8 = true; }
;     else if ((r -= IT_ATT) < IT_SSMO) { W = inp(KA, I_WSSMO) + (size_t)l * SW * D; WT = ws + WS_WCAT + (size_t)l * D * D; K = SW; N = D; Kd = D; kofs = AW; f8 = true; }
;     else if ((r -= IT_SSMO) < IT_OUT) { W = inp(KA, I_WOUT) + (size_t)l * D * D; WT = ws + WS_WOUT + (size_t)l * D * D; K = D; N = D; f8 = true; }
;     else if ((r -= IT_OUT) < NE * IT_W1) { const int e = r / IT_W1; r %= IT_W1; W = inp(KA, I_WEXPIN) + ((size_t)l * NE + e) * D * 2048; WT = ws + WS_W1 + ((size_t)l * NE + e) * 2048 * D; K = D; N = 2048; H = 1024; f8 = true; }
;     else { r -= NE * IT_W1; const int e = r / IT_W2; r %= IT_W2; W = inp(KA, I_WEXPOUT) + ((size_t)l * NE + e) * DFF * D; WT = ws + WS_W2 + ((size_t)l * NE + e) * D * DFF; K = DFF; N = D; f8 = true; }
;     const int nblk = N / 64, kb = r / nblk, nb = r % nblk, n0 = nb * 64;
;     d.W = W; d.WT = WT; d.N = N; d.Kd = Kd ? Kd : K; d.kofs = kofs; d.drow0 = (H ? imap(n0, H) : n0) - nsub; d.k0 = kb * 64; d.n0 = n0; d.f8 = f8;
.LBB0_575:
	s_add_i32 s8, s63, s95
	s_lshl_b32 s8, s8, 5
	s_or_b32 s8, s8, s100
	s_cmpk_lt_i32 s8, 0x6000
	s_cselect_b64 s[2:3], -1, 0
	s_and_b64 s[0:1], s[2:3], exec
	s_cselect_b32 s36, s8, 0
	s_add_i32 s0, s36, 0x680
	s_cmpk_gt_i32 s36, 0xfd7f
	s_mov_b64 s[18:19], -1
	s_cbranch_scc0 .LBB0_596
	s_mov_b64 s[42:43], -1
	s_cmpk_gt_u32 s0, 0x47f
	s_mov_b64 s[8:9], -1
	s_cbranch_scc0 .LBB0_593
	s_cmpk_gt_u32 s0, 0x4ff
	s_cbranch_scc0 .LBB0_590
	s_cmpk_gt_u32 s0, 0x57f
	s_cbranch_scc0 .LBB0_587
	s_cmp_lt_u32 s36, 0xfffff980
	s_cbranch_scc0 .LBB0_584
	s_mov_b64 s[28:29], -1
	s_cmpk_gt_u32 s0, 0x467f
	s_cbranch_scc0 .LBB0_582
	s_add_i32 s1, s36, 0xffffc000
	s_lshr_b32 s58, s1, 8
	s_load_dwordx2 s[8:9], s[6:7], 0xd0
	s_and_b32 s1, s36, 0xff
	s_lshl_b64 s[10:11], s[58:59], 20
	v_readlane_b32 s16, v255, 16
	v_readlane_b32 s17, v255, 17
	s_add_u32 s10, s10, s16
	s_addc_u32 s11, s11, s17
	s_lshl_b64 s[16:17], s[10:11], 2
	s_waitcnt lgkmcnt(0)
	s_add_u32 s16, s8, s16
	s_addc_u32 s17, s9, s17
	v_readlane_b32 s8, v253, 45
	s_add_u32 s10, s8, s10
	v_readlane_b32 s8, v253, 46
	s_addc_u32 s11, s8, s11
	s_mov_b64 s[8:9], 0

; DI const float* inp(kptr_t k, int i) { return (const float*)k[i]; }
; DI int imap(int n, int H) { return ((n % H) / 128) * 256 + (n / H) * 128 + (n % 128); }
; DI TItem decode_item(kptr_t KA, unsigned char* ws, int kind, int it) {
;     TItem d; d.valid = it < (kind == 0 ? DEPTH * IT_SMALL : IT_EXP); if (!d.valid) it = 0;
;     const int l = kind == 0 ? it / IT_SMALL : kind - 1; int r = kind == 0 ? it % IT_SMALL : IT_SMALL + it;
;     const float* W; unsigned char* WT; int K, N, H = 0; bool f8 = false;
;     int nsub = 0, Kd = 0, kofs = 0;
;     if (r < IT_IN) { W = inp(KA, I_WIN) + (size_t)l * D * INW; K = D; N = INW;
;         WT = ws + WS_WIN + (size_t)l * INW * D; f8 = true; }
;     else if ((r -= IT_IN) < IT_GLU) { W = inp(KA, I_WGLU) + (size_t)l * SW * 1024; WT = ws + WS_WGLU + (size_t)l * 1024 * SW * 2; K = SW; N = 1024; H = 512; }
;     else if ((r -= IT_GLU) < IT_ATT) { W = inp(KA, I_WATTO) + (size_t)l * AW * D; WT = ws + WS_WCAT + (size_t)l * D * D; K = AW; N = D; Kd = D; f8 = true; }
;     else if ((r -= IT_ATT) < IT_SSMO) { W = inp(KA, I_WSSMO) + (size_t)l * SW * D; WT = ws + WS_WCAT + (size_t)l * D * D; K = SW; N = D; Kd = D; kofs = AW; f8 = true; }
;     else if ((r -= IT_SSMO) < IT_OUT) { W = inp(KA, I_WOUT) + (size_t)l * D * D; WT = ws + WS_WOUT + (size_t)l * D * D; K = D; N = D; f8 = true; }
;     else if ((r -= IT_OUT) < NE * IT_W1) { const int e = r / IT_W1; r %= IT_W1; W = inp(KA, I_WEXPIN) + ((size_t)l * NE + e) * D * 2048; WT = ws + WS_W1 + ((size_t)l * NE + e) * 2048 * D; K = D; N = 2048; H = 1024; f8 = true; }
;     else { r -= NE * IT_W1; const int e = r / IT_W2; r %= IT_W2; W = inp(KA, I_WEXPOUT) + ((size_t)l * NE + e) * DFF * D; WT = ws + WS_W2 + ((size_t)l * NE + e) * D * DFF; K = DFF; N = D; f8 = true; }
;     const int nblk = N / 64, kb = r / nblk, nb = r % nblk, n0 = nb * 64;
;     d.W = W; d.WT = WT; d.N = N; d.Kd = Kd ? Kd : K; d.kofs = kofs; d.drow0 = (H ? imap(n0, H) : n0) - nsub; d.k0 = kb * 64; d.n0 = n0; d.f8 = f8;
.LBB0_609:
	s_add_i32 s9, s63, s95
	s_lshl_b32 s9, s9, 5
	s_or_b32 s9, s9, s100
	s_cmpk_lt_i32 s9, 0x6000
	s_cselect_b64 s[2:3], -1, 0
	s_and_b64 s[0:1], s[2:3], exec
	s_cselect_b32 s9, s9, 0
	s_add_i32 s0, s9, 0x680
	s_cmpk_gt_i32 s9, 0xfd7f
	s_mov_b64 s[18:19], -1
	s_cbranch_scc0 .LBB0_630
	s_mov_b64 s[16:17], -1
	s_cmpk_gt_u32 s0, 0x47f
	s_cbranch_scc0 .LBB0_627
	s_cmpk_gt_u32 s0, 0x4ff
	s_cbranch_scc0 .LBB0_624
	s_cmpk_gt_u32 s0, 0x57f
	s_cbranch_scc0 .LBB0_621
	s_cmp_lt_u32 s9, 0xfffff980
	s_cbranch_scc0 .LBB0_618
	s_mov_b64 s[78:79], -1
	s_cmpk_gt_u32 s0, 0x467f
	s_cbranch_scc0 .LBB0_616
	s_add_i32 s1, s9, 0xffffc000
	s_lshr_b32 s58, s1, 8
	s_load_dwordx2 s[18:19], s[6:7], 0xd0
	s_and_b32 s1, s9, 0xff
	s_lshl_b64 s[28:29], s[58:59], 20
	v_readlane_b32 s36, v255, 16
	v_readlane_b32 s37, v255, 17
	s_add_u32 s28, s28, s36
	s_addc_u32 s29, s29, s37
	s_lshl_b64 s[36:37], s[28:29], 2
	s_waitcnt lgkmcnt(0)
	s_add_u32 s56, s18, s36
	s_addc_u32 s57, s19, s37
	v_readlane_b32 s18, v253, 45
	s_add_u32 s28, s18, s28
	v_readlane_b32 s18, v253, 46
	s_addc_u32 s29, s18, s29
	s_mov_b64 s[18:19], 0

; DI const float* inp(kptr_t k, int i) { return (const float*)k[i]; }
; DI int imap(int n, int H) { return ((n % H) / 128) * 256 + (n / H) * 128 + (n % 128); }
; DI TItem decode_item(kptr_t KA, unsigned char* ws, int kind, int it) {
;     TItem d; d.valid = it < (kind == 0 ? DEPTH * IT_SMALL : IT_EXP); if (!d.valid) it = 0;
;     const int l = kind == 0 ? it / IT_SMALL : kind - 1; int r = kind == 0 ? it % IT_SMALL : IT_SMALL + it;
;     const float* W; unsigned char* WT; int K, N, H = 0; bool f8 = false;
;     int nsub = 0, Kd = 0, kofs = 0;
;     if (r < IT_IN) { W = inp(KA, I_WIN) + (size_t)l * D * INW; K = D; N = INW;
;         WT = ws + WS_WIN + (size_t)l * INW * D; f8 = true; }
;     else if ((r -= IT_IN) < IT_GLU) { W = inp(KA, I_WGLU) + (size_t)l * SW * 1024; WT = ws + WS_WGLU + (size_t)l * 1024 * SW * 2; K = SW; N = 1024; H = 512; }
;     else if ((r -= IT_GLU) < IT_ATT) { W = inp(KA, I_WATTO) + (size_t)l * AW * D; WT = ws + WS_WCAT + (size_t)l * D * D; K = AW; N = D; Kd = D; f8 = true; }
;     else if ((r -= IT_ATT) < IT_SSMO) { W = inp(KA, I_WSSMO) + (size_t)l * SW * D; WT = ws + WS_WCAT + (size_t)l * D * D; K = SW; N = D; Kd = D; kofs = AW; f8 = true; }
;     else if ((r -= IT_SSMO) < IT_OUT) { W = inp(KA, I_WOUT) + (size_t)l * D * D; WT = ws + WS_WOUT + (size_t)l * D * D; K = D; N = D; f8 = true; }
;     else if ((r -= IT_OUT) < NE * IT_W1) { const int e = r / IT_W1; r %= IT_W1; W = inp(KA, I_WEXPIN) + ((size_t)l * NE + e) * D * 2048; WT = ws + WS_W1 + ((size_t)l * NE + e) * 2048 * D; K = D; N = 2048; H = 1024; f8 = true; }
;     else { r -= NE * IT_W1; const int e = r / IT_W2; r %= IT_W2; W = inp(KA, I_WEXPOUT) + ((size_t)l * NE + e) * DFF * D; WT = ws + WS_W2 + ((size_t)l * NE + e) * D * DFF; K = DFF; N = D; f8 = true; }
;     const int nblk = N / 64, kb = r / nblk, nb = r % nblk, n0 = nb * 64;
;     d.W = W; d.WT = WT; d.N = N; d.Kd = Kd ? Kd : K; d.kofs = kofs; d.drow0 = (H ? imap(n0, H) : n0) - nsub; d.k0 = kb * 64; d.n0 = n0; d.f8 = f8;
.LBB0_651:
	s_add_i32 s4, s63, s95
	s_lshl_b32 s4, s4, 5
	s_or_b32 s4, s4, s100
	s_cmpk_lt_i32 s4, 0x6000
	s_cselect_b64 s[2:3], -1, 0
	s_and_b64 s[0:1], s[2:3], exec
	s_cselect_b32 s33, s4, 0
	s_add_i32 s0, s33, 0x680
	s_cmpk_gt_i32 s33, 0xfd7f
	s_mov_b64 s[18:19], -1
	s_cbranch_scc0 .LBB0_671
	s_mov_b64 s[8:9], -1
	s_cmpk_gt_u32 s0, 0x47f
	s_cbranch_scc0 .LBB0_668
	s_cmpk_gt_u32 s0, 0x4ff
	s_mov_b64 s[34:35], -1
	s_cbranch_scc0 .LBB0_665
	s_cmpk_gt_u32 s0, 0x57f
	s_cbranch_scc0 .LBB0_663
	s_cmp_lt_u32 s33, 0xfffff980
	s_cbranch_scc0 .LBB0_660
	s_mov_b64 s[28:29], -1
	s_cmpk_gt_u32 s0, 0x467f
	s_mov_b64 s[16:17], -1
	s_cbranch_scc0 .LBB0_658
	s_add_i32 s1, s33, 0xffffc000
	s_lshr_b32 s58, s1, 8
	s_load_dwordx2 s[4:5], s[6:7], 0xd0
	s_and_b32 s1, s33, 0xff
	s_lshl_b64 s[10:11], s[58:59], 20
	v_readlane_b32 s16, v255, 16
	v_readlane_b32 s17, v255, 17
	s_add_u32 s10, s10, s16
	s_addc_u32 s11, s11, s17
	s_lshl_b64 s[16:17], s[10:11], 2
	s_waitcnt lgkmcnt(0)
	s_add_u32 s4, s4, s16
	s_addc_u32 s5, s5, s17
	v_readlane_b32 s16, v253, 45
	s_add_u32 s10, s16, s10
	v_readlane_b32 s16, v253, 46
	s_addc_u32 s11, s16, s11
	s_mov_b64 s[16:17], 0

; DI const float* inp(kptr_t k, int i) { return (const float*)k[i]; }
; DI int imap(int n, int H) { return ((n % H) / 128) * 256 + (n / H) * 128 + (n % 128); }
; DI TItem decode_item(kptr_t KA, unsigned char* ws, int kind, int it) {
;     TItem d; d.valid = it < (kind == 0 ? DEPTH * IT_SMALL : IT_EXP); if (!d.valid) it = 0;
;     const int l = kind == 0 ? it / IT_SMALL : kind - 1; int r = kind == 0 ? it % IT_SMALL : IT_SMALL + it;
;     const float* W; unsigned char* WT; int K, N, H = 0; bool f8 = false;
;     int nsub = 0, Kd = 0, kofs = 0;
;     if (r < IT_IN) { W = inp(KA, I_WIN) + (size_t)l * D * INW; K = D; N = INW;
;         WT = ws + WS_WIN + (size_t)l * INW * D; f8 = true; }
;     else if ((r -= IT_IN) < IT_GLU) { W = inp(KA, I_WGLU) + (size_t)l * SW * 1024; WT = ws + WS_WGLU + (size_t)l * 1024 * SW * 2; K = SW; N = 1024; H = 512; }
;     else if ((r -= IT_GLU) < IT_ATT) { W = inp(KA, I_WATTO) + (size_t)l * AW * D; WT = ws + WS_WCAT + (size_t)l * D * D; K = AW; N = D; Kd = D; f8 = true; }
;     else if ((r -= IT_ATT) < IT_SSMO) { W = inp(KA, I_WSSMO) + (size_t)l * SW * D; WT = ws + WS_WCAT + (size_t)l * D * D; K = SW; N = D; Kd = D; kofs = AW; f8 = true; }
;     else if ((r -= IT_SSMO) < IT_OUT) { W = inp(KA, I_WOUT) + (size_t)l * D * D; WT = ws + WS_WOUT + (size_t)l * D * D; K = D; N = D; f8 = true; }
;     else if ((r -= IT_OUT) < NE * IT_W1) { const int e = r / IT_W1; r %= IT_W1; W = inp(KA, I_WEXPIN) + ((size_t)l * NE + e) * D * 2048; WT = ws + WS_W1 + ((size_t)l * NE + e) * 2048 * D; K = D; N = 2048; H = 1024; f8 = true; }
;     else { r -= NE * IT_W1; const int e = r / IT_W2; r %= IT_W2; W = inp(KA, I_WEXPOUT) + ((size_t)l * NE + e) * DFF * D; WT = ws + WS_W2 + ((size_t)l * NE + e) * D * DFF; K = DFF; N = D; f8 = true; }
;     const int nblk = N / 64, kb = r / nblk, nb = r % nblk, n0 = nb * 64;
;     d.W = W; d.WT = WT; d.N = N; d.Kd = Kd ? Kd : K; d.kofs = kofs; d.drow0 = (H ? imap(n0, H) : n0) - nsub; d.k0 = kb * 64; d.n0 = n0; d.f8 = f8;
.LBB0_684:
	s_xor_b64 s[34:35], s[8:9], -1
	s_add_i32 s2, s63, s95
	s_lshl_b32 s2, s2, 5
	s_or_b32 s2, s2, s100
	s_cmpk_gt_i32 s2, 0x5fff
	s_cselect_b64 s[16:17], -1, 0
	s_cmpk_lt_i32 s2, 0x6000
	s_cselect_b64 s[42:43], -1, 0
	s_and_b64 s[0:1], s[42:43], exec
	s_cselect_b32 s44, s2, 0
	s_add_i32 s1, s44, 0x680
	s_cmpk_gt_i32 s44, 0xfd7f
	s_mov_b64 s[18:19], -1
	s_cbranch_scc0 .LBB0_704
	s_mov_b64 s[8:9], -1
	s_cmpk_gt_u32 s1, 0x47f
	s_cbranch_scc0 .LBB0_701
	s_cmpk_gt_u32 s1, 0x4ff
	s_cbranch_scc0 .LBB0_698
	s_cmpk_gt_u32 s1, 0x57f
	s_mov_b64 s[2:3], -1
	s_cbranch_scc0 .LBB0_696
	s_cmp_lt_u32 s44, 0xfffff980
	s_cbranch_scc0 .LBB0_693
	s_mov_b64 s[36:37], -1
	s_cmpk_gt_u32 s1, 0x467f
	s_cbranch_scc0 .LBB0_691
	s_add_i32 s0, s44, 0xffffc000
	s_lshr_b32 s2, s0, 8
	s_load_dwordx2 s[18:19], s[6:7], 0xd0
	s_mov_b32 s3, s59
	s_and_b32 s39, s44, 0xff
	s_lshl_b64 s[2:3], s[2:3], 20
	v_readlane_b32 s28, v255, 16
	v_readlane_b32 s29, v255, 17
	s_add_u32 s2, s2, s28
	s_addc_u32 s3, s3, s29
	s_lshl_b64 s[28:29], s[2:3], 2
	s_waitcnt lgkmcnt(0)
	s_add_u32 s56, s18, s28
	s_addc_u32 s57, s19, s29
	v_readlane_b32 s0, v253, 45
	s_add_u32 s28, s0, s2
	v_readlane_b32 s0, v253, 46
	s_addc_u32 s29, s0, s3
	s_mov_b64 s[2:3], 0
